# topk table-row abs-max: one max per pair instead of canonicalise+max, v_max_f32_dpp reduction steps (on top of the rank/packed-add trims)
# speedup vs baseline: 1.0093x; 1.0037x over previous
.LBB0_1871:
	s_waitcnt vmcnt(16)
	v_max_f32_e64 v153, |v46|, |v47|
	v_max_f32_e64 v154, |v42|, |v43|
	v_max3_f32 v153, |v44|, |v45|, v153
	v_max3_f32 v154, |v40|, |v41|, v154
	v_max3_f32 v153, v153, 0, v154
	v_max_f32_e64 v154, |v38|, |v39|
	v_max_f32_e64 v155, |v34|, |v35|
	v_max3_f32 v154, |v36|, |v37|, v154
	v_max3_f32 v155, |v32|, |v33|, v155
	v_max3_f32 v153, v153, v154, v155
	s_waitcnt vmcnt(15)
	v_max_f32_e64 v154, |v50|, |v51|
	s_waitcnt vmcnt(12)
	v_max_f32_e64 v155, |v62|, |v63|
	v_max3_f32 v154, |v48|, |v49|, v154
	v_max3_f32 v155, |v60|, |v61|, v155
	v_max3_f32 v153, v153, v154, v155
	v_max_f32_e64 v154, |v58|, |v59|
	v_max_f32_e64 v155, |v54|, |v55|
	v_max3_f32 v154, |v56|, |v57|, v154
	v_max3_f32 v155, |v52|, |v53|, v155
	v_max3_f32 v153, v153, v154, v155
	s_mov_b32 s9, 0x42fe0000
	s_nop 1
	v_max_f32_dpp v153, v153, v153 row_ror:1 row_mask:0xf bank_mask:0xf
	s_nop 1
	v_max_f32_dpp v153, v153, v153 row_ror:2 row_mask:0xf bank_mask:0xf
	s_nop 1
	v_max_f32_dpp v153, v153, v153 row_ror:4 row_mask:0xf bank_mask:0xf
	s_nop 1
	v_max_f32_dpp v153, v153, v153 row_ror:8 row_mask:0xf bank_mask:0xf
	v_mov_b32_e32 v154, v153
	s_nop 1
	v_permlane16_swap_b32_e32 v153, v154
	v_max_f32_e32 v153, v153, v154
	v_mov_b32_e32 v154, v153
	s_nop 1
	v_permlane32_swap_b32_e32 v153, v154
	v_max_f32_e32 v153, v153, v154
	v_div_scale_f32 v154, s[52:53], v153, v153, s9
	v_rcp_f32_e32 v155, v154
	s_add_u32 s52, s92, s74
	s_addc_u32 s53, s93, s75
	v_fma_f32 v156, -v154, v155, 1.0
	v_fmac_f32_e32 v155, v156, v155
	v_div_scale_f32 v156, vcc, s9, v153, s9
	v_mul_f32_e32 v157, v156, v155
	v_fma_f32 v158, -v154, v157, v156
	v_fmac_f32_e32 v157, v158, v155
	v_fma_f32 v154, -v154, v157, v156
	v_div_fmas_f32 v154, v154, v155, v157
	v_div_fixup_f32 v154, v154, v153, s9
	v_cmp_lt_f32_e32 vcc, 0, v153
	s_mov_b32 s9, 0x40c0c00
	s_nop 0
	v_cndmask_b32_e32 v158, 0, v154, vcc
	v_pk_mul_f32 v[156:157], v[44:45], v[158:159] op_sel_hi:[1,0]
	v_pk_mul_f32 v[154:155], v[46:47], v[158:159] op_sel_hi:[1,0]
	v_pk_add_f32 v[156:157], v[156:157], v[242:243] op_sel_hi:[1,0]
	s_nop 0
	v_pk_add_f32 v[154:155], v[154:155], v[242:243] op_sel_hi:[1,0]
	v_perm_b32 v155, v155, v156, s9
	v_pk_mul_f32 v[160:161], v[40:41], v[158:159] op_sel_hi:[1,0]
	v_perm_b32 v230, v157, v155, v226
	v_perm_b32 v154, v154, v230, v228
	v_pk_mul_f32 v[156:157], v[42:43], v[158:159] op_sel_hi:[1,0]
	v_add_f32_e32 v159, 0x4b400000, v161
	v_add_f32_e32 v155, 0x4b400000, v160
	v_pk_add_f32 v[156:157], v[156:157], v[242:243] op_sel_hi:[1,0]
	v_perm_b32 v155, v157, v155, s9
	v_pk_mul_f32 v[160:161], v[36:37], v[158:159] op_sel_hi:[1,0]
	v_perm_b32 v230, v159, v155, v226
	v_perm_b32 v155, v156, v230, v228
	v_pk_mul_f32 v[156:157], v[38:39], v[158:159] op_sel_hi:[1,0]
	v_add_f32_e32 v159, 0x4b400000, v160
	v_add_f32_e32 v160, 0x4b400000, v161
	v_pk_add_f32 v[156:157], v[156:157], v[242:243] op_sel_hi:[1,0]
	v_perm_b32 v157, v157, v159, s9
	v_pk_mul_f32 v[162:163], v[32:33], v[158:159] op_sel_hi:[1,0]
	v_perm_b32 v230, v160, v157, v226
	v_perm_b32 v156, v156, v230, v228
	v_pk_mul_f32 v[160:161], v[34:35], v[158:159] op_sel_hi:[1,0]
	v_add_f32_e32 v159, 0x4b400000, v163
	v_add_f32_e32 v157, 0x4b400000, v162
	v_pk_add_f32 v[160:161], v[160:161], v[242:243] op_sel_hi:[1,0]
	s_nop 0
	v_perm_b32 v157, v161, v157, s9
	v_perm_b32 v230, v159, v157, v226
	v_perm_b32 v157, v160, v230, v228
	v_lshl_add_u64 v[160:161], v[130:131], 0, v[200:201]
	global_store_dwordx4 v[160:161], v[154:157], off
	v_pk_mul_f32 v[160:161], v[60:61], v[158:159] op_sel_hi:[1,0]
	s_nop 0
	v_pk_mul_f32 v[156:157], v[48:49], v[158:159] op_sel_hi:[1,0]
	v_pk_mul_f32 v[154:155], v[50:51], v[158:159] op_sel_hi:[1,0]
	v_pk_add_f32 v[156:157], v[156:157], v[242:243] op_sel_hi:[1,0]
	s_nop 0
	v_pk_add_f32 v[154:155], v[154:155], v[242:243] op_sel_hi:[1,0]
	v_perm_b32 v155, v155, v156, s9
	v_perm_b32 v230, v157, v155, v226
	v_perm_b32 v154, v154, v230, v228
	v_pk_mul_f32 v[156:157], v[62:63], v[158:159] op_sel_hi:[1,0]
	v_add_f32_e32 v159, 0x4b400000, v161
	v_add_f32_e32 v155, 0x4b400000, v160
	v_pk_add_f32 v[156:157], v[156:157], v[242:243] op_sel_hi:[1,0]
	v_perm_b32 v155, v157, v155, s9
	v_pk_mul_f32 v[160:161], v[56:57], v[158:159] op_sel_hi:[1,0]
	v_perm_b32 v230, v159, v155, v226
	v_perm_b32 v155, v156, v230, v228
	v_pk_mul_f32 v[156:157], v[58:59], v[158:159] op_sel_hi:[1,0]
	v_add_f32_e32 v159, 0x4b400000, v160
	v_add_f32_e32 v160, 0x4b400000, v161
	v_pk_add_f32 v[156:157], v[156:157], v[242:243] op_sel_hi:[1,0]
	s_nop 0
	s_nop 0
	v_perm_b32 v157, v157, v159, s9
	v_perm_b32 v230, v160, v157, v226
	v_perm_b32 v156, v156, v230, v228
	v_pk_mul_f32 v[160:161], v[54:55], v[158:159] op_sel_hi:[1,0]
	v_pk_mul_f32 v[158:159], v[52:53], v[158:159] op_sel_hi:[1,0]
	s_nop 0
	v_add_f32_e32 v157, 0x4b400000, v158
	v_add_f32_e32 v158, 0x4b400000, v159
	s_nop 0
	v_add_f32_e32 v159, 0x4b400000, v160
	v_add_f32_e32 v160, 0x4b400000, v161
	s_nop 0
	s_nop 0
	s_nop 0
	v_perm_b32 v157, v160, v157, s9
	v_perm_b32 v230, v158, v157, v226
	v_perm_b32 v157, v159, v230, v228
	v_lshl_add_u64 v[158:159], v[128:129], 0, v[200:201]
	global_store_dwordx4 v[158:159], v[154:157], off
	s_and_saveexec_b64 s[80:81], s[20:21]
	s_cbranch_execz .LBB0_1873
	v_mul_f32_e32 v153, 0x3c010204, v153
	v_mov_b32_e32 v154, 0x850000
	global_store_dword v154, v153, s[52:53]
.LBB0_1873:
	s_or_b64 exec, exec, s[80:81]
	s_waitcnt vmcnt(13)
	v_max_f32_e64 v153, |v66|, |v67|
	s_waitcnt vmcnt(10)
	v_max_f32_e64 v154, |v78|, |v79|
	v_max3_f32 v153, |v64|, |v65|, v153
	v_max3_f32 v154, |v76|, |v77|, v154
	v_max3_f32 v153, v153, 0, v154
	v_max_f32_e64 v154, |v74|, |v75|
	v_max_f32_e64 v155, |v70|, |v71|
	v_max3_f32 v154, |v72|, |v73|, v154
	v_max3_f32 v155, |v68|, |v69|, v155
	v_max3_f32 v153, v153, v154, v155
	s_waitcnt vmcnt(9)
	v_max_f32_e64 v154, |v82|, |v83|
	s_waitcnt vmcnt(6)
	v_max_f32_e64 v155, |v94|, |v95|
	v_max3_f32 v154, |v80|, |v81|, v154
	v_max3_f32 v155, |v92|, |v93|, v155
	v_max3_f32 v153, v153, v154, v155
	v_max_f32_e64 v154, |v90|, |v91|
	v_max_f32_e64 v155, |v86|, |v87|
	v_max3_f32 v154, |v88|, |v89|, v154
	v_max3_f32 v155, |v84|, |v85|, v155
	v_max3_f32 v153, v153, v154, v155
	s_mov_b32 s9, 0x42fe0000
	s_nop 1
	v_max_f32_dpp v153, v153, v153 row_ror:1 row_mask:0xf bank_mask:0xf
	s_nop 1
	v_max_f32_dpp v153, v153, v153 row_ror:2 row_mask:0xf bank_mask:0xf
	s_nop 1
	v_max_f32_dpp v153, v153, v153 row_ror:4 row_mask:0xf bank_mask:0xf
	s_nop 1
	v_max_f32_dpp v153, v153, v153 row_ror:8 row_mask:0xf bank_mask:0xf
	v_mov_b32_e32 v154, v153
	s_nop 1
	v_permlane16_swap_b32_e32 v153, v154
	v_max_f32_e32 v153, v153, v154
	v_mov_b32_e32 v154, v153
	s_nop 1
	v_permlane32_swap_b32_e32 v153, v154
	v_max_f32_e32 v153, v153, v154
	v_div_scale_f32 v154, s[80:81], v153, v153, s9
	v_rcp_f32_e32 v155, v154
	s_nop 0
	v_fma_f32 v156, -v154, v155, 1.0
	v_fmac_f32_e32 v155, v156, v155
	v_div_scale_f32 v156, vcc, s9, v153, s9
	v_mul_f32_e32 v157, v156, v155
	v_fma_f32 v158, -v154, v157, v156
	v_fmac_f32_e32 v157, v158, v155
	v_fma_f32 v154, -v154, v157, v156
	v_div_fmas_f32 v154, v154, v155, v157
	v_div_fixup_f32 v154, v154, v153, s9
	v_cmp_lt_f32_e32 vcc, 0, v153
	s_mov_b32 s9, 0x40c0c00
	s_nop 0
	v_cndmask_b32_e32 v158, 0, v154, vcc
	v_pk_mul_f32 v[156:157], v[64:65], v[158:159] op_sel_hi:[1,0]
	v_pk_mul_f32 v[154:155], v[66:67], v[158:159] op_sel_hi:[1,0]
	v_pk_add_f32 v[156:157], v[156:157], v[242:243] op_sel_hi:[1,0]
	s_nop 0
	v_pk_add_f32 v[154:155], v[154:155], v[242:243] op_sel_hi:[1,0]
	v_perm_b32 v155, v155, v156, s9
	v_pk_mul_f32 v[160:161], v[76:77], v[158:159] op_sel_hi:[1,0]
	v_perm_b32 v230, v157, v155, v226
	v_perm_b32 v154, v154, v230, v228
	v_pk_mul_f32 v[156:157], v[78:79], v[158:159] op_sel_hi:[1,0]
	v_add_f32_e32 v159, 0x4b400000, v161
	v_add_f32_e32 v155, 0x4b400000, v160
	v_pk_add_f32 v[156:157], v[156:157], v[242:243] op_sel_hi:[1,0]
	v_perm_b32 v155, v157, v155, s9
	v_pk_mul_f32 v[160:161], v[72:73], v[158:159] op_sel_hi:[1,0]
	v_perm_b32 v230, v159, v155, v226
	v_perm_b32 v155, v156, v230, v228
	v_pk_mul_f32 v[156:157], v[74:75], v[158:159] op_sel_hi:[1,0]
	v_add_f32_e32 v159, 0x4b400000, v160
	v_add_f32_e32 v160, 0x4b400000, v161
	v_pk_add_f32 v[156:157], v[156:157], v[242:243] op_sel_hi:[1,0]
	v_perm_b32 v157, v157, v159, s9
	v_pk_mul_f32 v[162:163], v[68:69], v[158:159] op_sel_hi:[1,0]
	v_perm_b32 v230, v160, v157, v226
	v_perm_b32 v156, v156, v230, v228
	v_pk_mul_f32 v[160:161], v[70:71], v[158:159] op_sel_hi:[1,0]
	v_add_f32_e32 v159, 0x4b400000, v163
	v_add_f32_e32 v157, 0x4b400000, v162
	v_pk_add_f32 v[160:161], v[160:161], v[242:243] op_sel_hi:[1,0]
	s_nop 0
	v_perm_b32 v157, v161, v157, s9
	v_perm_b32 v230, v159, v157, v226
	v_perm_b32 v157, v160, v230, v228
	v_lshl_add_u64 v[160:161], v[126:127], 0, v[200:201]
	global_store_dwordx4 v[160:161], v[154:157], off
	v_pk_mul_f32 v[160:161], v[92:93], v[158:159] op_sel_hi:[1,0]
	s_nop 0
	v_pk_mul_f32 v[156:157], v[80:81], v[158:159] op_sel_hi:[1,0]
	v_pk_mul_f32 v[154:155], v[82:83], v[158:159] op_sel_hi:[1,0]
	v_pk_add_f32 v[156:157], v[156:157], v[242:243] op_sel_hi:[1,0]
	s_nop 0
	v_pk_add_f32 v[154:155], v[154:155], v[242:243] op_sel_hi:[1,0]
	v_perm_b32 v155, v155, v156, s9
	v_perm_b32 v230, v157, v155, v226
	v_perm_b32 v154, v154, v230, v228
	v_pk_mul_f32 v[156:157], v[94:95], v[158:159] op_sel_hi:[1,0]
	v_add_f32_e32 v159, 0x4b400000, v161
	v_add_f32_e32 v155, 0x4b400000, v160
	v_pk_add_f32 v[156:157], v[156:157], v[242:243] op_sel_hi:[1,0]
	v_perm_b32 v155, v157, v155, s9
	v_pk_mul_f32 v[160:161], v[88:89], v[158:159] op_sel_hi:[1,0]
	v_perm_b32 v230, v159, v155, v226
	v_perm_b32 v155, v156, v230, v228
	v_pk_mul_f32 v[156:157], v[90:91], v[158:159] op_sel_hi:[1,0]
	v_add_f32_e32 v159, 0x4b400000, v160
	v_add_f32_e32 v160, 0x4b400000, v161
	v_pk_add_f32 v[156:157], v[156:157], v[242:243] op_sel_hi:[1,0]
	s_nop 0
	s_nop 0
	v_perm_b32 v157, v157, v159, s9
	v_perm_b32 v230, v160, v157, v226
	v_perm_b32 v156, v156, v230, v228
	v_pk_mul_f32 v[160:161], v[86:87], v[158:159] op_sel_hi:[1,0]
	v_pk_mul_f32 v[158:159], v[84:85], v[158:159] op_sel_hi:[1,0]
	s_nop 0
	v_add_f32_e32 v157, 0x4b400000, v158
	v_add_f32_e32 v158, 0x4b400000, v159
	s_nop 0
	v_add_f32_e32 v159, 0x4b400000, v160
	v_add_f32_e32 v160, 0x4b400000, v161
	s_nop 0
	s_nop 0
	s_nop 0
	v_perm_b32 v157, v160, v157, s9
	v_perm_b32 v230, v158, v157, v226
	v_perm_b32 v157, v159, v230, v228
	v_lshl_add_u64 v[158:159], v[124:125], 0, v[200:201]
	global_store_dwordx4 v[158:159], v[154:157], off
	s_and_saveexec_b64 s[80:81], s[20:21]
	s_cbranch_execz .LBB0_1846
	v_mul_f32_e32 v153, 0x3c010204, v153
	v_mov_b32_e32 v154, 0x890000
	global_store_dword v154, v153, s[52:53]
	s_branch .LBB0_1846
